# P3 projection output stores write-back (sc1 dropped): L2 absorbs the 32 MB per-round store burst
# speedup vs baseline: 1.0129x; 1.0129x over previous
; __device__ __forceinline__ float shx(float v, int o, int lane) { return __builtin_bit_cast(float, __builtin_amdgcn_ds_bpermute((lane ^ o) << 2, __builtin_bit_cast(int, v))); }
; __device__ __forceinline__ int fresh_lane() { int l; asm volatile("v_mbcnt_lo_u32_b32 %0, -1, 0\n\tv_mbcnt_hi_u32_b32 %0, -1, %0" : "=v"(l)); return l; }
; __device__ __forceinline__ void rows_rstd(const float* ssp, int row0, int fq, int ln, float (&rs)[8]) {
;     f32x4 a[8], b[8];
; #pragma unroll
;     for (int q = 0; q < 8; ++q) { const f32x4* p = (const f32x4*)(ssp + (size_t)(row0 + (q >> 2) * 128 + (q & 3) * 16) * 32 + 8 * fq); a[q] = p[0]; b[q] = p[1]; }
; #pragma unroll
;     for (int q = 0; q < 8; ++q) { float s = ((a[q].x + a[q].y) + (a[q].z + a[q].w)) + ((b[q].x + b[q].y) + (b[q].z + b[q].w));
;         s += shx(s, 16, ln); s += shx(s, 32, ln); rs[q] = rsqrtf(s * (1.0f / D) + RMS_EPS); }
; }
;     __device__ __forceinline__ void operator()(AccRef acc, const Unit& u, int wr, int wc, int, int) const {
;         const int ln_ = fresh_lane(), fr = ln_ & 15, fq = ln_ >> 4;
;         const int row0 = u.pm * 256 + wr * 64 + fr, col0 = u.pn * 256 + wc * 32 + 8 * fq;
;         const __amdgpu_buffer_rsrc_t rsrc = __builtin_amdgcn_make_buffer_rsrc((void*)O, 0, (int)((size_t)M * DINP * 2), 0x00020000);
;         float rs[8]; rows_rstd(ss, row0, fq, ln_, rs);
.LBB0_342:
	s_lshl_b32 s6, s6, 8
	v_mbcnt_lo_u32_b32 v178, -1, 0
	v_mbcnt_hi_u32_b32 v178, -1, v178
	s_add_i32 s6, s6, s38
	v_ashrrev_i32_e32 v130, 1, v178
	v_and_or_b32 v200, v178, 15, s6
	s_lshl_b32 s6, s7, 8
	v_and_b32_e32 v130, -8, v130
	s_or_b32 s6, s6, s39
	v_ashrrev_i32_e32 v131, 31, v130
	v_ashrrev_i32_e32 v201, 31, v200
	v_add_u32_e32 v209, s6, v130
	v_lshl_add_u64 v[130:131], v[130:131], 2, s[8:9]
	v_lshlrev_b64 v[132:133], 7, v[200:201]
	v_or_b32_e32 v134, 16, v200
	v_lshl_add_u64 v[132:133], v[130:131], 0, v[132:133]
	v_ashrrev_i32_e32 v135, 31, v134
	s_nop 0
	s_nop 0
	v_lshlrev_b64 v[134:135], 7, v[134:135]
	v_lshl_add_u64 v[134:135], v[130:131], 0, v[134:135]
	s_nop 0
	s_nop 0
	v_or_b32_e32 v134, 32, v200
	v_ashrrev_i32_e32 v135, 31, v134
	v_lshlrev_b64 v[134:135], 7, v[134:135]
	v_lshl_add_u64 v[134:135], v[130:131], 0, v[134:135]
	s_nop 0
	s_nop 0
	v_or_b32_e32 v134, 48, v200
	v_ashrrev_i32_e32 v135, 31, v134
	v_lshlrev_b64 v[134:135], 7, v[134:135]
	v_lshl_add_u64 v[130:131], v[130:131], 0, v[134:135]
	s_nop 0
	s_nop 0
	v_add_co_u32_e32 v134, vcc, s71, v132
	v_lshl_add_u64 v[130:131], v[132:133], 0, s[92:93]
	s_nop 0
	v_addc_co_u32_e32 v135, vcc, 0, v133, vcc
	v_add_co_u32_e32 v136, vcc, s72, v132
	s_mov_b64 s[6:7], 0x5000
	s_nop 0
	v_addc_co_u32_e32 v137, vcc, 0, v133, vcc
	s_nop 0
	s_nop 0
	v_lshl_add_u64 v[130:131], v[132:133], 0, s[94:95]
	s_nop 0
	s_nop 0
	v_lshl_add_u64 v[130:131], v[132:133], 0, s[6:7]
	s_nop 0
	s_nop 0
	s_mov_b64 s[6:7], 0x5800
	v_lshl_add_u64 v[130:131], v[132:133], 0, s[6:7]
	s_nop 0
	s_nop 0
	s_nop 0
	v_lshlrev_b32_e32 v178, 2, v178
	v_xor_b32_e32 v224, 64, v178
	v_xor_b32_e32 v201, 0x80, v178
	s_mov_b32 s6, 0x358637bd
	v_mov_b64_e32 v[206:207], s[6:7]
	s_mov_b32 s20, 0x3a000000
	s_mov_b32 s13, 0x800000
	s_nop 0
	v_mov_b32_e32 v178, v226
	v_mov_b32_e32 v179, v230
	v_mov_b32_e32 v230, v227
	v_mov_b32_e32 v180, v228
	v_mov_b32_e32 v181, v232
	v_mov_b32_e32 v232, v229
	v_pk_add_f32 v[178:179], v[178:179], v[230:231]
	v_pk_add_f32 v[180:181], v[180:181], v[232:233]
	v_mov_b32_e32 v182, v236
	v_pk_add_f32 v[178:179], v[178:179], v[180:181]
	v_mov_b32_e32 v180, v234
	v_mov_b32_e32 v181, v238
	v_mov_b32_e32 v238, v235
	v_mov_b32_e32 v183, v240
	v_mov_b32_e32 v240, v237
	v_pk_add_f32 v[180:181], v[180:181], v[238:239]
	v_pk_add_f32 v[182:183], v[182:183], v[240:241]
	s_nop 0
	v_pk_add_f32 v[180:181], v[180:181], v[182:183]
	v_mov_b32_e32 v183, v178
	v_mov_b32_e32 v182, v180
	v_mov_b32_e32 v178, v181
	v_pk_add_f32 v[178:179], v[182:183], v[178:179]
	ds_bpermute_b32 v181, v224, v179
	ds_bpermute_b32 v180, v224, v178
	s_waitcnt lgkmcnt(0)
	v_pk_add_f32 v[178:179], v[178:179], v[180:181]
	ds_bpermute_b32 v181, v201, v179
	ds_bpermute_b32 v180, v201, v178
	s_waitcnt lgkmcnt(0)
	v_pk_add_f32 v[178:179], v[178:179], v[180:181]
	s_nop 0
	v_pk_fma_f32 v[178:179], v[178:179], s[20:21], v[206:207] op_sel_hi:[1,0,0]
	s_nop 0
	v_mul_f32_e32 v180, 0x4b800000, v179
	v_cmp_gt_f32_e64 s[6:7], s13, v179
	v_cmp_gt_f32_e32 vcc, s13, v178
	s_nop 0
	v_cndmask_b32_e64 v179, v179, v180, s[6:7]
	v_rsq_f32_e32 v179, v179
	s_nop 0
	v_mul_f32_e32 v180, 0x45800000, v179
	v_cndmask_b32_e64 v204, v179, v180, s[6:7]
	v_mov_b32_e32 v204, v242
	v_mul_f32_e32 v179, 0x4b800000, v178
	v_cndmask_b32_e32 v178, v178, v179, vcc
	v_rsq_f32_e32 v178, v178
	v_pk_mul_f32 v[128:129], v[128:129], v[204:205] op_sel_hi:[1,0]
	v_pk_mul_f32 v[126:127], v[126:127], v[204:205] op_sel_hi:[1,0]
	v_pk_mul_f32 v[120:121], v[120:121], v[204:205] op_sel_hi:[1,0]
	v_mul_f32_e32 v179, 0x45800000, v178
	v_cndmask_b32_e32 v202, v178, v179, vcc
	v_mov_b32_e32 v202, v243
	v_mov_b32_e32 v178, v170
	v_mov_b32_e32 v179, v174
	v_mov_b32_e32 v174, v171
	v_pk_add_f32 v[170:171], v[178:179], v[174:175]
	v_mov_b32_e32 v174, v172
	v_mov_b32_e32 v175, v176
	v_mov_b32_e32 v176, v173
	v_pk_add_f32 v[172:173], v[174:175], v[176:177]
	v_pk_mul_f32 v[118:119], v[118:119], v[204:205] op_sel_hi:[1,0]
	v_pk_add_f32 v[170:171], v[170:171], v[172:173]
	v_mov_b32_e32 v172, v166
	v_mov_b32_e32 v173, v162
	v_mov_b32_e32 v162, v167
	v_mov_b32_e32 v166, v168
	v_mov_b32_e32 v167, v164
	v_mov_b32_e32 v164, v169
	v_pk_add_f32 v[162:163], v[172:173], v[162:163]
	v_pk_add_f32 v[164:165], v[166:167], v[164:165]
	v_mov_b32_e32 v166, v158
	v_pk_add_f32 v[162:163], v[162:163], v[164:165]
	v_mov_b32_e32 v165, v170
	v_mov_b32_e32 v164, v162
	v_mov_b32_e32 v170, v163
	v_pk_add_f32 v[162:163], v[164:165], v[170:171]
	ds_bpermute_b32 v165, v224, v163
	ds_bpermute_b32 v164, v224, v162
	v_mov_b32_e32 v167, v154
	v_mov_b32_e32 v154, v159
	v_mov_b32_e32 v158, v160
	v_mov_b32_e32 v159, v156
	v_mov_b32_e32 v156, v161
	v_pk_add_f32 v[154:155], v[166:167], v[154:155]
	v_pk_add_f32 v[156:157], v[158:159], v[156:157]
	s_waitcnt lgkmcnt(0)
	v_pk_add_f32 v[162:163], v[162:163], v[164:165]
	v_pk_add_f32 v[154:155], v[154:155], v[156:157]
	v_mov_b32_e32 v156, v150
	v_mov_b32_e32 v157, v146
	v_mov_b32_e32 v146, v151
	v_mov_b32_e32 v150, v152
	v_mov_b32_e32 v151, v148
	v_mov_b32_e32 v148, v153
	v_pk_add_f32 v[146:147], v[156:157], v[146:147]
	v_pk_add_f32 v[148:149], v[150:151], v[148:149]
	ds_bpermute_b32 v165, v201, v163
	v_pk_add_f32 v[146:147], v[146:147], v[148:149]
	v_mov_b32_e32 v149, v154
	v_mov_b32_e32 v148, v146
	v_mov_b32_e32 v154, v147
	ds_bpermute_b32 v164, v201, v162
	v_pk_add_f32 v[146:147], v[148:149], v[154:155]
	ds_bpermute_b32 v149, v224, v147
	ds_bpermute_b32 v148, v224, v146
	v_mov_b32_e32 v150, v142
	v_mov_b32_e32 v151, v138
	v_mov_b32_e32 v138, v143
	v_mov_b32_e32 v142, v144
	v_mov_b32_e32 v143, v140
	v_mov_b32_e32 v140, v145
	v_pk_add_f32 v[138:139], v[150:151], v[138:139]
	v_pk_add_f32 v[140:141], v[142:143], v[140:141]
	s_waitcnt lgkmcnt(2)
; __device__ __forceinline__ unsigned cvt_pk_bf16(float lo, float hi) { unsigned r; asm volatile("v_cvt_pk_bf16_f32 %0, %1, %2" : "=v"(r) : "v"(lo), "v"(hi)); return r; }
; __device__ __forceinline__ float shx(float v, int o, int lane) { return __builtin_bit_cast(float, __builtin_amdgcn_ds_bpermute((lane ^ o) << 2, __builtin_bit_cast(int, v))); }
; __device__ __forceinline__ void store16_wt(__amdgpu_buffer_rsrc_t rsrc, unsigned byte_off, v4u v) { __builtin_amdgcn_raw_buffer_store_b128(v, rsrc, byte_off, 0, 16); }
; __device__ __forceinline__ void rows_rstd(const float* ssp, int row0, int fq, int ln, float (&rs)[8]) {
;     ...
;     for (int q = 0; q < 8; ++q) { float s = ((a[q].x + a[q].y) + (a[q].z + a[q].w)) + ((b[q].x + b[q].y) + (b[q].z + b[q].w));
;         s += shx(s, 16, ln); s += shx(s, 32, ln); rs[q] = rsqrtf(s * (1.0f / D) + RMS_EPS); }
;     __device__ __forceinline__ void operator()(AccRef acc, const Unit& u, int wr, int wc, int, int) const {
;     ...
;         for (int ai = 0; ai < 2; ++ai)
; #pragma unroll
;             for (int m = 0; m < 4; ++m) {
;                 const int row = row0 + ai * 128 + m * 16;
;                 const float r = rs[ai * 4 + m];
; #pragma unroll
;                 for (int bj = 0; bj < 2; ++bj) {
;                     const f32x4 v0 = acc[ai][bj][m][0] * r, v1 = acc[ai][bj][m][1] * r;
;                     v4u w; w.x = cvt_pk_bf16(v0[0], v0[1]); w.y = cvt_pk_bf16(v0[2], v0[3]); w.z = cvt_pk_bf16(v1[0], v1[1]); w.w = cvt_pk_bf16(v1[2], v1[3]);
;                     store16_wt(rsrc, (unsigned)(((size_t)row * DINP + col0 + bj * 128) * 2), w);
;                 }
	v_pk_add_f32 v[162:163], v[162:163], v[164:165]
	v_pk_add_f32 v[138:139], v[138:139], v[140:141]
	v_mov_b32_e32 v140, v134
	v_mov_b32_e32 v141, v130
	v_mov_b32_e32 v130, v135
	v_mov_b32_e32 v134, v136
	v_mov_b32_e32 v135, v132
	v_mov_b32_e32 v132, v137
	v_pk_add_f32 v[130:131], v[140:141], v[130:131]
	v_pk_add_f32 v[132:133], v[134:135], v[132:133]
	v_pk_fma_f32 v[162:163], v[162:163], s[20:21], v[206:207] op_sel_hi:[1,0,0]
	v_pk_add_f32 v[130:131], v[130:131], v[132:133]
	s_waitcnt lgkmcnt(0)
	v_pk_add_f32 v[146:147], v[146:147], v[148:149]
	v_mov_b32_e32 v132, v130
	v_mov_b32_e32 v133, v138
	v_mov_b32_e32 v138, v131
	v_mul_f32_e32 v164, 0x4b800000, v163
	v_cmp_gt_f32_e64 s[6:7], s13, v163
	ds_bpermute_b32 v149, v201, v147
	ds_bpermute_b32 v148, v201, v146
	v_pk_add_f32 v[130:131], v[132:133], v[138:139]
	v_cndmask_b32_e64 v163, v163, v164, s[6:7]
	ds_bpermute_b32 v133, v224, v131
	ds_bpermute_b32 v132, v224, v130
	v_rsq_f32_e32 v163, v163
	s_waitcnt lgkmcnt(2)
	v_pk_add_f32 v[146:147], v[146:147], v[148:149]
	v_cmp_gt_f32_e32 vcc, s13, v162
	v_pk_fma_f32 v[146:147], v[146:147], s[20:21], v[206:207] op_sel_hi:[1,0,0]
	v_mul_f32_e32 v164, 0x45800000, v163
	s_waitcnt lgkmcnt(0)
	v_pk_add_f32 v[130:131], v[130:131], v[132:133]
	v_cndmask_b32_e64 v164, v163, v164, s[6:7]
	v_mov_b32_e32 v164, v244
	v_mul_f32_e32 v163, 0x4b800000, v162
	v_mul_f32_e32 v148, 0x4b800000, v147
	v_cmp_gt_f32_e64 s[6:7], s13, v147
	ds_bpermute_b32 v133, v201, v131
	ds_bpermute_b32 v132, v201, v130
	v_cndmask_b32_e32 v162, v162, v163, vcc
	v_cndmask_b32_e64 v147, v147, v148, s[6:7]
	v_rsq_f32_e32 v162, v162
	v_rsq_f32_e32 v147, v147
	s_waitcnt lgkmcnt(0)
	v_pk_add_f32 v[130:131], v[130:131], v[132:133]
	v_pk_mul_f32 v[134:135], v[124:125], v[204:205] op_sel_hi:[1,0]
	v_mul_f32_e32 v163, 0x45800000, v162
	v_mul_f32_e32 v148, 0x45800000, v147
	v_pk_fma_f32 v[130:131], v[130:131], s[20:21], v[206:207] op_sel_hi:[1,0,0]
	v_cndmask_b32_e32 v162, v162, v163, vcc
	v_mov_b32_e32 v162, v245
	v_cmp_gt_f32_e32 vcc, s13, v146
	v_cndmask_b32_e64 v148, v147, v148, s[6:7]
	v_mov_b32_e32 v148, v246
	v_mul_f32_e32 v147, 0x4b800000, v146
	v_mul_f32_e32 v132, 0x4b800000, v131
	v_cmp_gt_f32_e64 s[6:7], s13, v131
	v_cndmask_b32_e32 v146, v146, v147, vcc
	v_rsq_f32_e32 v146, v146
	v_cndmask_b32_e64 v131, v131, v132, s[6:7]
	v_rsq_f32_e32 v131, v131
	v_readlane_b32 s20, v254, 19
	v_mul_f32_e32 v147, 0x45800000, v146
	v_cndmask_b32_e32 v146, v146, v147, vcc
	v_mov_b32_e32 v146, v247
	v_mul_f32_e32 v132, 0x45800000, v131
	v_cmp_gt_f32_e32 vcc, s13, v130
	v_cndmask_b32_e64 v132, v131, v132, s[6:7]
	v_mov_b32_e32 v132, v248
	v_mul_f32_e32 v131, 0x4b800000, v130
	v_cndmask_b32_e32 v130, v130, v131, vcc
	v_rsq_f32_e32 v130, v130
	s_movk_i32 s6, 0x3c00
	v_pk_mul_f32 v[124:125], v[122:123], v[204:205] op_sel_hi:[1,0]
	v_cvt_pk_bf16_f32 v122, v126, v127
	v_mul_f32_e32 v131, 0x45800000, v130
	v_cndmask_b32_e32 v130, v130, v131, vcc
	v_mov_b32_e32 v130, v249
	v_mul_lo_u32 v131, v200, s6
	v_add_lshl_u32 v131, v209, v131, 1
	v_cvt_pk_bf16_f32 v123, v128, v129
	v_readlane_b32 s21, v254, 20
	v_readlane_b32 s22, v254, 21
	v_readlane_b32 s23, v254, 22
	v_cvt_pk_bf16_f32 v124, v124, v125
	v_cvt_pk_bf16_f32 v125, v134, v135
	v_pk_mul_f32 v[104:105], v[104:105], v[202:203] op_sel_hi:[1,0]
	v_pk_mul_f32 v[102:103], v[102:103], v[202:203] op_sel_hi:[1,0]
	v_pk_mul_f32 v[88:89], v[88:89], v[164:165] op_sel_hi:[1,0]
	s_nop 1
	buffer_store_dwordx4 v[122:125], v131, s[20:23], 0 offen
	v_pk_mul_f32 v[86:87], v[86:87], v[164:165] op_sel_hi:[1,0]
	v_pk_mul_f32 v[72:73], v[72:73], v[162:163] op_sel_hi:[1,0]
	v_pk_mul_f32 v[122:123], v[112:113], v[204:205] op_sel_hi:[1,0]
	v_pk_mul_f32 v[112:113], v[110:111], v[204:205] op_sel_hi:[1,0]
	v_cvt_pk_bf16_f32 v110, v118, v119
	v_cvt_pk_bf16_f32 v111, v120, v121
	v_add_u32_e32 v118, 0x78000, v131
	v_cvt_pk_bf16_f32 v112, v112, v113
	v_cvt_pk_bf16_f32 v113, v122, v123
	buffer_store_dwordx4 v[110:113], v131, s[20:23], 0 offen offset:256
	v_pk_mul_f32 v[70:71], v[70:71], v[162:163] op_sel_hi:[1,0]
	v_pk_mul_f32 v[64:65], v[64:65], v[148:149] op_sel_hi:[1,0]
	v_pk_mul_f32 v[110:111], v[116:117], v[202:203] op_sel_hi:[1,0]
	v_pk_mul_f32 v[112:113], v[114:115], v[202:203] op_sel_hi:[1,0]
	v_pk_mul_f32 v[114:115], v[108:109], v[202:203] op_sel_hi:[1,0]
	v_pk_mul_f32 v[108:109], v[106:107], v[202:203] op_sel_hi:[1,0]
	v_cvt_pk_bf16_f32 v106, v112, v113
	v_cvt_pk_bf16_f32 v107, v110, v111
	v_pk_mul_f32 v[62:63], v[62:63], v[148:149] op_sel_hi:[1,0]
	v_cvt_pk_bf16_f32 v108, v108, v109
	v_cvt_pk_bf16_f32 v109, v114, v115
	buffer_store_dwordx4 v[106:109], v118, s[20:23], 0 offen
	v_pk_mul_f32 v[56:57], v[56:57], v[148:149] op_sel_hi:[1,0]
	v_pk_mul_f32 v[54:55], v[54:55], v[148:149] op_sel_hi:[1,0]
	v_pk_mul_f32 v[106:107], v[96:97], v[202:203] op_sel_hi:[1,0]
	v_pk_mul_f32 v[96:97], v[94:95], v[202:203] op_sel_hi:[1,0]
	v_cvt_pk_bf16_f32 v94, v102, v103
	v_cvt_pk_bf16_f32 v95, v104, v105
	v_add_u32_e32 v102, 0xf0000, v131
	v_cvt_pk_bf16_f32 v96, v96, v97
	v_cvt_pk_bf16_f32 v97, v106, v107
	buffer_store_dwordx4 v[94:97], v118, s[20:23], 0 offen offset:256
	v_pk_mul_f32 v[40:41], v[40:41], v[146:147] op_sel_hi:[1,0]
; __device__ __forceinline__ unsigned cvt_pk_bf16(float lo, float hi) { unsigned r; asm volatile("v_cvt_pk_bf16_f32 %0, %1, %2" : "=v"(r) : "v"(lo), "v"(hi)); return r; }
; __device__ __forceinline__ void store16_wt(__amdgpu_buffer_rsrc_t rsrc, unsigned byte_off, v4u v) { __builtin_amdgcn_raw_buffer_store_b128(v, rsrc, byte_off, 0, 16); }
;     __device__ __forceinline__ void operator()(AccRef acc, const Unit& u, int wr, int wc, int, int) const {
;     ...
;         for (int ai = 0; ai < 2; ++ai)
; #pragma unroll
;             for (int m = 0; m < 4; ++m) {
;                 const int row = row0 + ai * 128 + m * 16;
;                 const float r = rs[ai * 4 + m];
; #pragma unroll
;                 for (int bj = 0; bj < 2; ++bj) {
;                     const f32x4 v0 = acc[ai][bj][m][0] * r, v1 = acc[ai][bj][m][1] * r;
;                     v4u w; w.x = cvt_pk_bf16(v0[0], v0[1]); w.y = cvt_pk_bf16(v0[2], v0[3]); w.z = cvt_pk_bf16(v1[0], v1[1]); w.w = cvt_pk_bf16(v1[2], v1[3]);
;                     store16_wt(rsrc, (unsigned)(((size_t)row * DINP + col0 + bj * 128) * 2), w);
;                 }
	v_pk_mul_f32 v[38:39], v[38:39], v[146:147] op_sel_hi:[1,0]
	v_pk_mul_f32 v[94:95], v[100:101], v[164:165] op_sel_hi:[1,0]
	v_pk_mul_f32 v[96:97], v[98:99], v[164:165] op_sel_hi:[1,0]
	v_pk_mul_f32 v[98:99], v[92:93], v[164:165] op_sel_hi:[1,0]
	v_pk_mul_f32 v[92:93], v[90:91], v[164:165] op_sel_hi:[1,0]
	v_cvt_pk_bf16_f32 v90, v96, v97
	v_cvt_pk_bf16_f32 v91, v94, v95
	v_pk_mul_f32 v[24:25], v[24:25], v[132:133] op_sel_hi:[1,0]
	v_cvt_pk_bf16_f32 v92, v92, v93
	v_cvt_pk_bf16_f32 v93, v98, v99
	buffer_store_dwordx4 v[90:93], v102, s[20:23], 0 offen
	v_pk_mul_f32 v[22:23], v[22:23], v[132:133] op_sel_hi:[1,0]
	s_mov_b64 s[6:7], -1
	v_pk_mul_f32 v[90:91], v[80:81], v[164:165] op_sel_hi:[1,0]
	v_pk_mul_f32 v[80:81], v[78:79], v[164:165] op_sel_hi:[1,0]
	v_cvt_pk_bf16_f32 v78, v86, v87
	v_cvt_pk_bf16_f32 v79, v88, v89
	v_add_u32_e32 v86, 0x168000, v131
	v_cvt_pk_bf16_f32 v80, v80, v81
	v_cvt_pk_bf16_f32 v81, v90, v91
	buffer_store_dwordx4 v[78:81], v102, s[20:23], 0 offen offset:256
	s_andn2_b64 vcc, exec, s[4:5]
	v_pk_mul_f32 v[6:7], v[6:7], v[130:131] op_sel_hi:[1,0]
	v_pk_mul_f32 v[78:79], v[84:85], v[162:163] op_sel_hi:[1,0]
	v_pk_mul_f32 v[80:81], v[82:83], v[162:163] op_sel_hi:[1,0]
	v_pk_mul_f32 v[82:83], v[76:77], v[162:163] op_sel_hi:[1,0]
	v_pk_mul_f32 v[76:77], v[74:75], v[162:163] op_sel_hi:[1,0]
	v_cvt_pk_bf16_f32 v74, v80, v81
	v_cvt_pk_bf16_f32 v75, v78, v79
	v_pk_mul_f32 v[4:5], v[4:5], v[130:131] op_sel_hi:[1,0]
	v_cvt_pk_bf16_f32 v76, v76, v77
	v_cvt_pk_bf16_f32 v77, v82, v83
	buffer_store_dwordx4 v[74:77], v86, s[20:23], 0 offen
	s_nop 1
	v_pk_mul_f32 v[74:75], v[68:69], v[162:163] op_sel_hi:[1,0]
	v_pk_mul_f32 v[68:69], v[66:67], v[162:163] op_sel_hi:[1,0]
	v_cvt_pk_bf16_f32 v66, v70, v71
	v_cvt_pk_bf16_f32 v67, v72, v73
	s_nop 0
	v_cvt_pk_bf16_f32 v68, v68, v69
	v_cvt_pk_bf16_f32 v69, v74, v75
	buffer_store_dwordx4 v[66:69], v86, s[20:23], 0 offen offset:256
	s_nop 1
	v_add_u32_e32 v68, 0x3c0000, v131
	v_pk_mul_f32 v[66:67], v[60:61], v[148:149] op_sel_hi:[1,0]
	v_pk_mul_f32 v[60:61], v[58:59], v[148:149] op_sel_hi:[1,0]
	v_cvt_pk_bf16_f32 v58, v62, v63
	v_cvt_pk_bf16_f32 v59, v64, v65
	s_nop 0
	v_cvt_pk_bf16_f32 v60, v60, v61
	v_cvt_pk_bf16_f32 v61, v66, v67
	buffer_store_dwordx4 v[58:61], v68, s[20:23], 0 offen
	s_nop 1
	v_pk_mul_f32 v[58:59], v[48:49], v[148:149] op_sel_hi:[1,0]
	v_pk_mul_f32 v[48:49], v[46:47], v[148:149] op_sel_hi:[1,0]
	v_cvt_pk_bf16_f32 v46, v54, v55
	v_cvt_pk_bf16_f32 v47, v56, v57
	v_add_u32_e32 v54, 0x438000, v131
	v_cvt_pk_bf16_f32 v48, v48, v49
	v_cvt_pk_bf16_f32 v49, v58, v59
	buffer_store_dwordx4 v[46:49], v68, s[20:23], 0 offen offset:256
	s_nop 1
	v_pk_mul_f32 v[46:47], v[52:53], v[146:147] op_sel_hi:[1,0]
	v_pk_mul_f32 v[48:49], v[50:51], v[146:147] op_sel_hi:[1,0]
	v_pk_mul_f32 v[50:51], v[44:45], v[146:147] op_sel_hi:[1,0]
	v_pk_mul_f32 v[44:45], v[42:43], v[146:147] op_sel_hi:[1,0]
	v_cvt_pk_bf16_f32 v42, v48, v49
	v_cvt_pk_bf16_f32 v43, v46, v47
	s_nop 0
	v_cvt_pk_bf16_f32 v44, v44, v45
	v_cvt_pk_bf16_f32 v45, v50, v51
	buffer_store_dwordx4 v[42:45], v54, s[20:23], 0 offen
	s_nop 1
	v_pk_mul_f32 v[42:43], v[32:33], v[146:147] op_sel_hi:[1,0]
	v_pk_mul_f32 v[32:33], v[30:31], v[146:147] op_sel_hi:[1,0]
	v_cvt_pk_bf16_f32 v30, v38, v39
	v_cvt_pk_bf16_f32 v31, v40, v41
	v_add_u32_e32 v38, 0x4b0000, v131
	v_cvt_pk_bf16_f32 v32, v32, v33
	v_cvt_pk_bf16_f32 v33, v42, v43
	buffer_store_dwordx4 v[30:33], v54, s[20:23], 0 offen offset:256
	s_nop 1
	v_pk_mul_f32 v[30:31], v[36:37], v[132:133] op_sel_hi:[1,0]
	v_pk_mul_f32 v[32:33], v[34:35], v[132:133] op_sel_hi:[1,0]
	v_pk_mul_f32 v[34:35], v[28:29], v[132:133] op_sel_hi:[1,0]
	v_pk_mul_f32 v[28:29], v[26:27], v[132:133] op_sel_hi:[1,0]
	v_cvt_pk_bf16_f32 v26, v32, v33
	v_cvt_pk_bf16_f32 v27, v30, v31
	s_nop 0
	v_cvt_pk_bf16_f32 v28, v28, v29
	v_cvt_pk_bf16_f32 v29, v34, v35
	buffer_store_dwordx4 v[26:29], v38, s[20:23], 0 offen
	s_nop 1
	v_pk_mul_f32 v[26:27], v[16:17], v[132:133] op_sel_hi:[1,0]
	v_pk_mul_f32 v[16:17], v[14:15], v[132:133] op_sel_hi:[1,0]
	v_cvt_pk_bf16_f32 v14, v22, v23
	v_cvt_pk_bf16_f32 v15, v24, v25
	v_add_u32_e32 v22, 0x528000, v131
	v_cvt_pk_bf16_f32 v16, v16, v17
	v_cvt_pk_bf16_f32 v17, v26, v27
	buffer_store_dwordx4 v[14:17], v38, s[20:23], 0 offen offset:256
	s_nop 1
	v_pk_mul_f32 v[14:15], v[20:21], v[130:131] op_sel_hi:[1,0]
	v_pk_mul_f32 v[16:17], v[18:19], v[130:131] op_sel_hi:[1,0]
	v_pk_mul_f32 v[18:19], v[12:13], v[130:131] op_sel_hi:[1,0]
	v_pk_mul_f32 v[12:13], v[10:11], v[130:131] op_sel_hi:[1,0]
	v_cvt_pk_bf16_f32 v10, v16, v17
	v_cvt_pk_bf16_f32 v11, v14, v15
	s_nop 0
	v_cvt_pk_bf16_f32 v12, v12, v13
	v_cvt_pk_bf16_f32 v13, v18, v19
	buffer_store_dwordx4 v[10:13], v22, s[20:23], 0 offen
	s_nop 1
	v_pk_mul_f32 v[10:11], v[2:3], v[130:131] op_sel_hi:[1,0]
	v_pk_mul_f32 v[2:3], v[0:1], v[130:131] op_sel_hi:[1,0]
	v_cvt_pk_bf16_f32 v0, v4, v5
	v_cvt_pk_bf16_f32 v1, v6, v7
	s_nop 0
	v_cvt_pk_bf16_f32 v2, v2, v3
	v_cvt_pk_bf16_f32 v3, v10, v11
	buffer_store_dwordx4 v[0:3], v22, s[20:23], 0 offen offset:256
	s_cbranch_vccnz .LBB0_335
	s_andn2_b64 vcc, exec, s[0:1]
	s_cbranch_vccnz .LBB0_334
	s_barrier
	s_branch .LBB0_334
